# final6 + in-proj (e4m3 layers) epilogue: second row-block's RMS partial loads issued together with the first block's (one exposed L2 round trip instead of two)
# baseline (speedup 1.0000x reference)
; DI float sum_x16(float v, int lane) { return v + bpx(v, lane, 16); }
; DI float sum_x32(float v, int lane) { return v + bpx(v, lane, 32); }
; __device__ __forceinline__ void rowscale4(const float* part, size_t rowb, int fq, int lane, float (&sc)[4]) {
;     f32x4 a[4], b[4];
; #pragma unroll
;     for (int m = 0; m < 4; ++m) { const f32x4* p = (const f32x4*)(part + (rowb + 16 * m) * 32 + fq * 8); a[m] = p[0]; b[m] = p[1]; }
; #pragma unroll
;     for (int m = 0; m < 4; ++m) { float s = ((a[m].x + a[m].y) + (a[m].z + a[m].w)) + ((b[m].x + b[m].y) + (b[m].z + b[m].w));
;         s = sum_x32(sum_x16(s, lane), lane); sc[m] = rsqrtf(s * (1.f / D) + EPS); }
; }
;     __device__ __forceinline__ void operator()(const f32x4 (&acc)[2][2][4][2], const Unit& u, int wr, int wc, int fr, int fq) const {
;         const int row0 = u.pm * BM + wr * 64 + fr, col0 = u.pn * BM + wc * 32 + 8 * fq;
;         bf16_t* base = O + (size_t)(u.z >> zs) * o1 + (size_t)(u.z & zm) * o2;
; #pragma unroll
;         for (int ai = 0; ai < 2; ++ai) {
;             float sc[4] = {1.f, 1.f, 1.f, 1.f};
;             if (SC == 1) rowscale4(rv, (size_t)u.z * rvz + row0 + ai * HALF, fq, fr + 16 * fq, sc);
;             if constexpr (INP8) { const float cs = (u.pn < 4 ? SC_A : ((u.pn >= 12 && u.pn < 16) ? SC_B : 1.f)) * (1.f / W8S);
; #pragma unroll
;                 for (int m = 0; m < 4; ++m) sc[m] *= cs; }
.LBB0_704:
	s_mov_b32 s42, s53
	s_add_u32 s84, s55, 0xffffff00
	s_nop 15
	s_nop 15
	s_addc_u32 s85, s94, -1
	v_mbcnt_lo_u32_b32 v2, -1, s42
	v_mbcnt_hi_u32_b32 v2, -1, v2
	s_lshl_b32 s42, s44, 8
	v_and_b32_e32 v5, 15, v2
	s_add_i32 s42, s42, s31
	v_ashrrev_i32_e32 v6, 4, v2
	v_or_b32_e32 v18, s42, v5
	s_lshl_b32 s42, s11, 8
	v_lshlrev_b32_e32 v2, 3, v6
	s_or_b32 s42, s42, s35
	v_add_u32_e32 v4, s42, v2
	v_lshlrev_b32_e32 v6, 6, v6
	v_lshlrev_b32_e32 v5, 2, v5
	s_movk_i32 s42, 0x80
	v_ashrrev_i32_e32 v19, 31, v18
	v_ashrrev_i32_e32 v3, 31, v2
	v_bitop3_b32 v27, v6, 64, v5 bitop3:0x36
	v_bitop3_b32 v26, v6, s42, v5 bitop3:0x36
	v_ashrrev_i32_e32 v5, 31, v4
	v_lshl_add_u64 v[20:21], v[4:5], 1, s[46:47]
	v_lshl_add_u64 v[2:3], v[2:3], 2, s[48:49]
	v_lshlrev_b64 v[4:5], 7, v[18:19]
	v_lshl_add_u64 v[22:23], v[2:3], 0, v[4:5]
	global_load_dwordx4 v[28:31], v[22:23], off
	global_load_dwordx4 v[168:171], v[22:23], off offset:16
	global_load_dwordx4 v[172:175], v[22:23], off offset:2048
	global_load_dwordx4 v[180:183], v[22:23], off offset:2064
	v_add_co_u32_e32 v4, vcc, s10, v22
	s_mov_b64 s[42:43], 0x1000
	s_nop 0
	v_addc_co_u32_e32 v5, vcc, 0, v23, vcc
	v_lshl_add_u64 v[2:3], v[22:23], 0, s[42:43]
	global_load_dwordx4 v[10:13], v[4:5], off
	global_load_dwordx4 v[14:17], v[2:3], off offset:16
	s_mov_b64 s[42:43], 0x1800
	v_lshl_add_u64 v[2:3], v[22:23], 0, s[42:43]
	global_load_dwordx4 v[6:9], v[4:5], off offset:2048
	s_nop 0
	global_load_dwordx4 v[2:5], v[2:3], off offset:16
	s_mov_b64 s[100:101], 0x4000
	v_lshl_add_u64 v[244:245], v[22:23], 0, s[100:101]
	global_load_dwordx4 v[206:209], v[244:245], off
	global_load_dwordx4 v[210:213], v[244:245], off offset:16
	global_load_dwordx4 v[214:217], v[244:245], off offset:2048
	global_load_dwordx4 v[218:221], v[244:245], off offset:2064
	s_mov_b64 s[100:101], 0x5000
	v_lshl_add_u64 v[244:245], v[22:23], 0, s[100:101]
	global_load_dwordx4 v[232:235], v[244:245], off
	global_load_dwordx4 v[236:239], v[244:245], off offset:16
	global_load_dwordx4 v[184:187], v[244:245], off offset:2048
	global_load_dwordx4 v[240:243], v[244:245], off offset:2064
	s_mov_b32 s42, 0x358637bd
	s_mov_b32 s76, 0x3a000000
	s_mov_b32 s55, 0x800000
	s_mov_b32 s97, 0x24000
	s_mov_b32 s87, 0x10000
	s_waitcnt vmcnt(0)
	v_mov_b32_e32 v24, v28
	v_mov_b32_e32 v25, v168
	v_mov_b32_e32 v168, v29
	v_mov_b32_e32 v28, v30
	v_mov_b32_e32 v29, v170
	v_mov_b32_e32 v170, v31
	v_pk_add_f32 v[24:25], v[24:25], v[168:169]
	v_pk_add_f32 v[28:29], v[28:29], v[170:171]
	v_mov_b32_e32 v30, v174
	v_pk_add_f32 v[24:25], v[24:25], v[28:29]
	v_mov_b32_e32 v28, v172
	v_mov_b32_e32 v29, v180
	v_mov_b32_e32 v180, v173
	v_mov_b32_e32 v31, v182
	v_mov_b32_e32 v182, v175
	v_pk_add_f32 v[28:29], v[28:29], v[180:181]
	v_pk_add_f32 v[30:31], v[30:31], v[182:183]
	s_nop 0
	v_pk_add_f32 v[28:29], v[28:29], v[30:31]
	v_mov_b32_e32 v31, v24
	v_mov_b32_e32 v30, v28
	v_mov_b32_e32 v24, v29
	v_pk_add_f32 v[24:25], v[30:31], v[24:25]
	ds_bpermute_b32 v29, v27, v25
	ds_bpermute_b32 v28, v27, v24
	s_waitcnt lgkmcnt(0)
	v_pk_add_f32 v[24:25], v[24:25], v[28:29]
	ds_bpermute_b32 v29, v26, v25
	ds_bpermute_b32 v28, v26, v24
	s_waitcnt lgkmcnt(0)
	v_pk_add_f32 v[28:29], v[24:25], v[28:29]
	v_mov_b64_e32 v[24:25], s[42:43]
	v_pk_fma_f32 v[28:29], v[28:29], s[76:77], v[24:25] op_sel_hi:[1,0,0]
	s_nop 0
	v_mul_f32_e32 v19, 0x4b800000, v29
	v_cmp_gt_f32_e64 s[42:43], s55, v29
	v_cmp_gt_f32_e32 vcc, s55, v28
	s_nop 0
	v_cndmask_b32_e64 v19, v29, v19, s[42:43]
	v_rsq_f32_e32 v19, v19
	s_nop 0
	v_mul_f32_e32 v29, 0x45800000, v19
	v_cndmask_b32_e64 v19, v19, v29, s[42:43]
	v_mul_f32_e32 v29, 0x4b800000, v28
	v_cndmask_b32_e32 v28, v28, v29, vcc
	v_rsq_f32_e32 v28, v28
	s_nop 0
	v_mul_f32_e32 v29, 0x45800000, v28
	v_cndmask_b32_e32 v30, v28, v29, vcc
	v_mov_b32_e32 v28, v10
	v_mov_b32_e32 v29, v14
	v_mov_b32_e32 v14, v11
	v_pk_add_f32 v[10:11], v[28:29], v[14:15]
	v_mov_b32_e32 v14, v12
	v_mov_b32_e32 v15, v16
	v_mov_b32_e32 v16, v13
	v_pk_add_f32 v[12:13], v[14:15], v[16:17]
	s_nop 0
	v_pk_add_f32 v[10:11], v[10:11], v[12:13]
	v_mov_b32_e32 v12, v6
	v_mov_b32_e32 v13, v2
	v_mov_b32_e32 v2, v7
	v_mov_b32_e32 v6, v8
	v_mov_b32_e32 v7, v4
	v_mov_b32_e32 v4, v9
	v_pk_add_f32 v[2:3], v[12:13], v[2:3]
	v_pk_add_f32 v[4:5], v[6:7], v[4:5]
	s_nop 0
	v_pk_add_f32 v[2:3], v[2:3], v[4:5]
	v_mov_b32_e32 v5, v10
	v_mov_b32_e32 v4, v2
	v_mov_b32_e32 v10, v3
	v_pk_add_f32 v[2:3], v[4:5], v[10:11]
	ds_bpermute_b32 v5, v27, v3
	ds_bpermute_b32 v4, v27, v2
	s_waitcnt lgkmcnt(0)
	v_pk_add_f32 v[2:3], v[2:3], v[4:5]
	ds_bpermute_b32 v5, v26, v3
	ds_bpermute_b32 v4, v26, v2
	s_waitcnt lgkmcnt(0)
; DI float sum_x16(float v, int lane) { return v + bpx(v, lane, 16); }
; __device__ __forceinline__ void rowscale4(const float* part, size_t rowb, int fq, int lane, float (&sc)[4]) {
;     f32x4 a[4], b[4];
; #pragma unroll
;     for (int m = 0; m < 4; ++m) { const f32x4* p = (const f32x4*)(part + (rowb + 16 * m) * 32 + fq * 8); a[m] = p[0]; b[m] = p[1]; }
; #pragma unroll
;     for (int m = 0; m < 4; ++m) { float s = ((a[m].x + a[m].y) + (a[m].z + a[m].w)) + ((b[m].x + b[m].y) + (b[m].z + b[m].w));
;         s = sum_x32(sum_x16(s, lane), lane); sc[m] = rsqrtf(s * (1.f / D) + EPS); }
; }
;     __device__ __forceinline__ void operator()(const f32x4 (&acc)[2][2][4][2], const Unit& u, int wr, int wc, int fr, int fq) const {
;     ...
;             float sc[4] = {1.f, 1.f, 1.f, 1.f};
;             if (SC == 1) rowscale4(rv, (size_t)u.z * rvz + row0 + ai * HALF, fq, fr + 16 * fq, sc);
;             if constexpr (INP8) { const float cs = (u.pn < 4 ? SC_A : ((u.pn >= 12 && u.pn < 16) ? SC_B : 1.f)) * (1.f / W8S);
; #pragma unroll
;                 for (int m = 0; m < 4; ++m) sc[m] *= cs; }
;             if (SC == 2) {
; #pragma unroll
;                 for (int m = 0; m < 4; ++m) sc[m] = rv[(size_t)u.z * rvz + row0 + ai * HALF + m * 16]; }
; #pragma unroll
;             for (int m = 0; m < 4; ++m) { const int row = row0 + ai * HALF + m * 16;
;                 bf16_t* rowp = base + (size_t)row * ldc + col0;
;                 if constexpr (V8) { { unsigned char* rp8 = (unsigned char*)O + (size_t)(u.z >> zs) * o1 + (size_t)(u.z & zm) * o2 + (size_t)row * ldc + col0; const float s8m = sc[m] * s8;
; #pragma unroll
;                     for (int bj = 0; bj < 2; ++bj) { const f32x4 v0 = acc[ai][bj][m][0] * s8m, v1 = acc[ai][bj][m][1] * s8m;
;                         u32x2 w8; w8.x = pk8(clamp8(v0[0]), clamp8(v0[1]), clamp8(v0[2]), clamp8(v0[3])); w8.y = pk8(clamp8(v1[0]), clamp8(v1[1]), clamp8(v1[2]), clamp8(v1[3]));
;                         *(u32x2*)(rp8 + bj * HALF) = w8; }
;                     continue; } }
; #pragma unroll
;                 for (int bj = 0; bj < 2; ++bj) { const f32x4 v0 = acc[ai][bj][m][0] * sc[m], v1 = acc[ai][bj][m][1] * sc[m];
;                     u32x4 w; w.x = cvt_pk_bf16(v0[0], v0[1]); w.y = cvt_pk_bf16(v0[2], v0[3]); w.z = cvt_pk_bf16(v1[0], v1[1]); w.w = cvt_pk_bf16(v1[2], v1[3]);
;                     *(u32x4*)(rowp + bj * HALF) = w; } } }
	v_pk_add_f32 v[2:3], v[2:3], v[4:5]
	s_nop 0
	v_pk_fma_f32 v[2:3], v[2:3], s[76:77], v[24:25] op_sel_hi:[1,0,0]
	v_mov_b32_e32 v5, 0x3b38aa3b
	v_mul_f32_e32 v4, 0x4b800000, v3
	v_cmp_gt_f32_e64 s[42:43], s55, v3
	v_cmp_gt_f32_e32 vcc, s55, v2
	s_nop 0
	v_cndmask_b32_e64 v3, v3, v4, s[42:43]
	v_rsq_f32_e32 v3, v3
	s_nop 0
	v_mul_f32_e32 v4, 0x45800000, v3
	v_cndmask_b32_e64 v3, v3, v4, s[42:43]
	v_mul_f32_e32 v4, 0x4b800000, v2
	v_cndmask_b32_e32 v2, v2, v4, vcc
	v_rsq_f32_e32 v2, v2
	s_and_b32 s42, s11, -4
	s_cmp_eq_u32 s42, 12
	v_mad_i64_i32 v[14:15], s[42:43], v18, s17, v[20:21]
	v_mul_f32_e32 v4, 0x45800000, v2
	v_cndmask_b32_e32 v2, v2, v4, vcc
	s_cselect_b64 vcc, -1, 0
	v_mov_b32_e32 v4, 0x3c800000
	s_cmp_gt_i32 s11, 3
	v_cndmask_b32_e32 v4, v4, v5, vcc
	s_cselect_b64 vcc, -1, 0
	v_mov_b32_e32 v5, 0x3b0293ee
	v_cndmask_b32_e32 v163, v5, v4, vcc
	v_mul_f32_e32 v6, v163, v19
	v_mul_f32_e32 v10, v163, v3
	v_mul_f32_e32 v12, v163, v2
	v_pk_mul_f32 v[2:3], v[158:159], v[6:7] op_sel_hi:[1,0]
	v_pk_mul_f32 v[4:5], v[160:161], v[6:7] op_sel_hi:[1,0]
	v_cvt_pk_bf16_f32 v2, v2, v3
	v_pk_mul_f32 v[16:17], v[156:157], v[6:7] op_sel_hi:[1,0]
	v_cvt_pk_bf16_f32 v3, v4, v5
	v_pk_mul_f32 v[28:29], v[154:155], v[6:7] op_sel_hi:[1,0]
	v_mul_f32_e32 v8, v163, v30
	v_cvt_pk_bf16_f32 v4, v28, v29
	v_cvt_pk_bf16_f32 v5, v16, v17
	global_store_dwordx4 v[14:15], v[2:5], off
	v_pk_mul_f32 v[16:17], v[124:125], v[6:7] op_sel_hi:[1,0]
	s_nop 0
	v_pk_mul_f32 v[2:3], v[126:127], v[6:7] op_sel_hi:[1,0]
	v_pk_mul_f32 v[4:5], v[128:129], v[6:7] op_sel_hi:[1,0]
	v_cvt_pk_bf16_f32 v2, v2, v3
	v_pk_mul_f32 v[6:7], v[122:123], v[6:7] op_sel_hi:[1,0]
	v_cvt_pk_bf16_f32 v3, v4, v5
	s_nop 0
	v_cvt_pk_bf16_f32 v4, v6, v7
	v_cvt_pk_bf16_f32 v5, v16, v17
	global_store_dwordx4 v[14:15], v[2:5], off offset:256
	v_pk_mul_f32 v[14:15], v[148:149], v[8:9] op_sel_hi:[1,0]
	v_pk_mul_f32 v[16:17], v[146:147], v[8:9] op_sel_hi:[1,0]
	v_or_b32_e32 v2, 16, v18
	v_mad_i64_i32 v[6:7], s[42:43], v2, s17, v[20:21]
	v_pk_mul_f32 v[2:3], v[150:151], v[8:9] op_sel_hi:[1,0]
	v_pk_mul_f32 v[4:5], v[152:153], v[8:9] op_sel_hi:[1,0]
	v_cvt_pk_bf16_f32 v2, v2, v3
	s_nop 0
	v_cvt_pk_bf16_f32 v3, v4, v5
	v_cvt_pk_bf16_f32 v4, v16, v17
	v_cvt_pk_bf16_f32 v5, v14, v15
	global_store_dwordx4 v[6:7], v[2:5], off
	v_pk_mul_f32 v[14:15], v[116:117], v[8:9] op_sel_hi:[1,0]
	s_nop 0
	v_pk_mul_f32 v[2:3], v[118:119], v[8:9] op_sel_hi:[1,0]
	v_pk_mul_f32 v[4:5], v[120:121], v[8:9] op_sel_hi:[1,0]
	v_cvt_pk_bf16_f32 v2, v2, v3
	v_pk_mul_f32 v[8:9], v[114:115], v[8:9] op_sel_hi:[1,0]
	v_cvt_pk_bf16_f32 v3, v4, v5
	s_nop 0
	v_cvt_pk_bf16_f32 v4, v8, v9
	v_cvt_pk_bf16_f32 v5, v14, v15
	global_store_dwordx4 v[6:7], v[2:5], off offset:256
	v_pk_mul_f32 v[8:9], v[140:141], v[10:11] op_sel_hi:[1,0]
	v_pk_mul_f32 v[14:15], v[138:139], v[10:11] op_sel_hi:[1,0]
	v_or_b32_e32 v2, 32, v18
	v_mad_i64_i32 v[6:7], s[42:43], v2, s17, v[20:21]
	v_pk_mul_f32 v[2:3], v[142:143], v[10:11] op_sel_hi:[1,0]
	v_pk_mul_f32 v[4:5], v[144:145], v[10:11] op_sel_hi:[1,0]
	v_cvt_pk_bf16_f32 v2, v2, v3
	s_nop 0
	v_cvt_pk_bf16_f32 v3, v4, v5
	v_cvt_pk_bf16_f32 v4, v14, v15
	v_cvt_pk_bf16_f32 v5, v8, v9
	global_store_dwordx4 v[6:7], v[2:5], off
	v_pk_mul_f32 v[8:9], v[108:109], v[10:11] op_sel_hi:[1,0]
	s_nop 0
	v_pk_mul_f32 v[2:3], v[110:111], v[10:11] op_sel_hi:[1,0]
	v_pk_mul_f32 v[4:5], v[112:113], v[10:11] op_sel_hi:[1,0]
	v_cvt_pk_bf16_f32 v2, v2, v3
	v_pk_mul_f32 v[10:11], v[106:107], v[10:11] op_sel_hi:[1,0]
	v_cvt_pk_bf16_f32 v3, v4, v5
	s_nop 0
	v_cvt_pk_bf16_f32 v4, v10, v11
	v_cvt_pk_bf16_f32 v5, v8, v9
	global_store_dwordx4 v[6:7], v[2:5], off offset:256
	v_pk_mul_f32 v[8:9], v[132:133], v[12:13] op_sel_hi:[1,0]
	v_pk_mul_f32 v[10:11], v[130:131], v[12:13] op_sel_hi:[1,0]
	v_or_b32_e32 v2, 48, v18
	v_mad_i64_i32 v[6:7], s[42:43], v2, s17, v[20:21]
	v_pk_mul_f32 v[4:5], v[136:137], v[12:13] op_sel_hi:[1,0]
	v_pk_mul_f32 v[2:3], v[134:135], v[12:13] op_sel_hi:[1,0]
	s_mov_b64 s[42:43], 0x4000
	v_cvt_pk_bf16_f32 v2, v2, v3
	v_cvt_pk_bf16_f32 v3, v4, v5
	v_cvt_pk_bf16_f32 v4, v10, v11
	v_cvt_pk_bf16_f32 v5, v8, v9
	global_store_dwordx4 v[6:7], v[2:5], off
	v_pk_mul_f32 v[10:11], v[98:99], v[12:13] op_sel_hi:[1,0]
	v_pk_mul_f32 v[8:9], v[100:101], v[12:13] op_sel_hi:[1,0]
	v_pk_mul_f32 v[4:5], v[104:105], v[12:13] op_sel_hi:[1,0]
	v_pk_mul_f32 v[2:3], v[102:103], v[12:13] op_sel_hi:[1,0]
	s_nop 0
	v_cvt_pk_bf16_f32 v2, v2, v3
	v_cvt_pk_bf16_f32 v3, v4, v5
	v_cvt_pk_bf16_f32 v4, v10, v11
	v_add_co_u32_e32 v10, vcc, s62, v22
	v_cvt_pk_bf16_f32 v5, v8, v9
	global_store_dwordx4 v[6:7], v[2:5], off offset:256
	v_lshl_add_u64 v[6:7], v[22:23], 0, s[42:43]
	v_addc_co_u32_e32 v11, vcc, 0, v23, vcc
	s_movk_i32 s42, 0x5000
	v_add_co_u32_e32 v32, vcc, s42, v22
	s_mov_b64 s[42:43], 0x4800
	s_nop 0
	v_addc_co_u32_e32 v33, vcc, 0, v23, vcc
	v_mov_b64_e32 v[2:3], v[206:207]
	v_mov_b64_e32 v[4:5], v[208:209]
	s_nop 0
	v_mov_b64_e32 v[6:7], v[210:211]
	v_mov_b64_e32 v[8:9], v[212:213]
	v_lshl_add_u64 v[14:15], v[22:23], 0, s[42:43]
	v_mov_b64_e32 v[10:11], v[214:215]
	v_mov_b64_e32 v[12:13], v[216:217]
	s_nop 0
	v_mov_b64_e32 v[14:15], v[218:219]
	v_mov_b64_e32 v[16:17], v[220:221]
	s_mov_b64 s[42:43], 0x5000
	v_lshl_add_u64 v[168:169], v[22:23], 0, s[42:43]
	v_mov_b64_e32 v[28:29], v[232:233]
	v_mov_b64_e32 v[30:31], v[234:235]
	s_nop 0
	v_mov_b64_e32 v[168:169], v[236:237]
	v_mov_b64_e32 v[170:171], v[238:239]
	s_mov_b64 s[42:43], 0x5800
	v_lshl_add_u64 v[22:23], v[22:23], 0, s[42:43]
	v_mov_b64_e32 v[172:173], v[184:185]
	v_mov_b64_e32 v[174:175], v[186:187]
	v_mov_b64_e32 v[180:181], v[240:241]
	v_mov_b64_e32 v[182:183], v[242:243]
	v_mov_b32_e32 v22, v2
	v_mov_b32_e32 v23, v6
	v_mov_b32_e32 v6, v3
	v_pk_add_f32 v[2:3], v[22:23], v[6:7]
	v_mov_b32_e32 v6, v4
	v_mov_b32_e32 v7, v8
	v_mov_b32_e32 v8, v5
	v_pk_add_f32 v[4:5], v[6:7], v[8:9]
	v_mov_b32_e32 v6, v12
	v_pk_add_f32 v[2:3], v[2:3], v[4:5]
	v_mov_b32_e32 v4, v10
	v_mov_b32_e32 v5, v14
	v_mov_b32_e32 v14, v11
	v_mov_b32_e32 v7, v16
	v_mov_b32_e32 v16, v13
	v_pk_add_f32 v[4:5], v[4:5], v[14:15]
	v_pk_add_f32 v[6:7], v[6:7], v[16:17]
	s_nop 0
	v_pk_add_f32 v[4:5], v[4:5], v[6:7]
	v_mov_b32_e32 v7, v2
	v_mov_b32_e32 v6, v4
	v_mov_b32_e32 v2, v5
	v_pk_add_f32 v[2:3], v[6:7], v[2:3]
	ds_bpermute_b32 v5, v27, v3
	ds_bpermute_b32 v4, v27, v2
	v_mov_b32_e32 v6, v174
	v_mov_b32_e32 v7, v182
	v_mov_b32_e32 v182, v175
	v_pk_add_f32 v[6:7], v[6:7], v[182:183]
	s_waitcnt lgkmcnt(0)
; DI float sum_x16(float v, int lane) { return v + bpx(v, lane, 16); }
; __device__ __forceinline__ void rowscale4(const float* part, size_t rowb, int fq, int lane, float (&sc)[4]) {
;     f32x4 a[4], b[4];
; #pragma unroll
;     for (int m = 0; m < 4; ++m) { const f32x4* p = (const f32x4*)(part + (rowb + 16 * m) * 32 + fq * 8); a[m] = p[0]; b[m] = p[1]; }
; #pragma unroll
;     for (int m = 0; m < 4; ++m) { float s = ((a[m].x + a[m].y) + (a[m].z + a[m].w)) + ((b[m].x + b[m].y) + (b[m].z + b[m].w));
;         s = sum_x32(sum_x16(s, lane), lane); sc[m] = rsqrtf(s * (1.f / D) + EPS); }
; }
;     __device__ __forceinline__ void operator()(const f32x4 (&acc)[2][2][4][2], const Unit& u, int wr, int wc, int fr, int fq) const {
;     ...
;             float sc[4] = {1.f, 1.f, 1.f, 1.f};
;             if (SC == 1) rowscale4(rv, (size_t)u.z * rvz + row0 + ai * HALF, fq, fr + 16 * fq, sc);
;             if constexpr (INP8) { const float cs = (u.pn < 4 ? SC_A : ((u.pn >= 12 && u.pn < 16) ? SC_B : 1.f)) * (1.f / W8S);
; #pragma unroll
;                 for (int m = 0; m < 4; ++m) sc[m] *= cs; }
;             if (SC == 2) {
; #pragma unroll
;                 for (int m = 0; m < 4; ++m) sc[m] = rv[(size_t)u.z * rvz + row0 + ai * HALF + m * 16]; }
; #pragma unroll
;             for (int m = 0; m < 4; ++m) { const int row = row0 + ai * HALF + m * 16;
;                 bf16_t* rowp = base + (size_t)row * ldc + col0;
;                 if constexpr (V8) { { unsigned char* rp8 = (unsigned char*)O + (size_t)(u.z >> zs) * o1 + (size_t)(u.z & zm) * o2 + (size_t)row * ldc + col0; const float s8m = sc[m] * s8;
; #pragma unroll
;                     for (int bj = 0; bj < 2; ++bj) { const f32x4 v0 = acc[ai][bj][m][0] * s8m, v1 = acc[ai][bj][m][1] * s8m;
;                         u32x2 w8; w8.x = pk8(clamp8(v0[0]), clamp8(v0[1]), clamp8(v0[2]), clamp8(v0[3])); w8.y = pk8(clamp8(v1[0]), clamp8(v1[1]), clamp8(v1[2]), clamp8(v1[3]));
;                         *(u32x2*)(rp8 + bj * HALF) = w8; }
;                     continue; } }
; #pragma unroll
;                 for (int bj = 0; bj < 2; ++bj) { const f32x4 v0 = acc[ai][bj][m][0] * sc[m], v1 = acc[ai][bj][m][1] * sc[m];
;                     u32x4 w; w.x = cvt_pk_bf16(v0[0], v0[1]); w.y = cvt_pk_bf16(v0[2], v0[3]); w.z = cvt_pk_bf16(v1[0], v1[1]); w.w = cvt_pk_bf16(v1[2], v1[3]);
;                     *(u32x4*)(rowp + bj * HALF) = w; } } }
	v_pk_add_f32 v[2:3], v[2:3], v[4:5]
	ds_bpermute_b32 v5, v26, v3
	ds_bpermute_b32 v4, v26, v2
	s_waitcnt lgkmcnt(0)
	v_pk_add_f32 v[2:3], v[2:3], v[4:5]
	s_nop 0
	v_pk_fma_f32 v[2:3], v[2:3], s[76:77], v[24:25] op_sel_hi:[1,0,0]
	v_mov_b32_e32 v5, v170
	v_mul_f32_e32 v4, 0x4b800000, v3
	v_cmp_gt_f32_e64 s[42:43], s55, v3
	v_cmp_gt_f32_e32 vcc, s55, v2
	v_mov_b32_e32 v170, v31
	v_cndmask_b32_e64 v3, v3, v4, s[42:43]
	v_rsq_f32_e32 v3, v3
	s_nop 0
	v_mul_f32_e32 v4, 0x45800000, v3
	v_cndmask_b32_e64 v8, v3, v4, s[42:43]
	v_mul_f32_e32 v3, 0x4b800000, v2
	v_cndmask_b32_e32 v2, v2, v3, vcc
	v_rsq_f32_e32 v2, v2
	v_mov_b32_e32 v4, v30
	v_pk_add_f32 v[4:5], v[4:5], v[170:171]
	v_mul_f32_e32 v3, 0x45800000, v2
	v_cndmask_b32_e32 v9, v2, v3, vcc
	v_mov_b32_e32 v2, v28
	v_mov_b32_e32 v3, v168
	v_mov_b32_e32 v168, v29
	v_pk_add_f32 v[2:3], v[2:3], v[168:169]
	s_nop 0
	v_pk_add_f32 v[2:3], v[2:3], v[4:5]
	v_mov_b32_e32 v4, v172
	v_mov_b32_e32 v5, v180
	v_mov_b32_e32 v180, v173
	v_pk_add_f32 v[4:5], v[4:5], v[180:181]
	s_nop 0
	v_pk_add_f32 v[4:5], v[4:5], v[6:7]
	v_mov_b32_e32 v7, v2
	v_mov_b32_e32 v6, v4
	v_mov_b32_e32 v2, v5
	v_pk_add_f32 v[2:3], v[6:7], v[2:3]
	ds_bpermute_b32 v5, v27, v3
	ds_bpermute_b32 v4, v27, v2
	v_mul_f32_e32 v6, v163, v8
	v_pk_mul_f32 v[16:17], v[92:93], v[6:7] op_sel_hi:[1,0]
	v_pk_mul_f32 v[22:23], v[90:91], v[6:7] op_sel_hi:[1,0]
	v_mul_f32_e32 v8, v163, v9
	s_waitcnt lgkmcnt(0)
	v_pk_add_f32 v[2:3], v[2:3], v[4:5]
	ds_bpermute_b32 v5, v26, v3
	ds_bpermute_b32 v4, v26, v2
	s_waitcnt lgkmcnt(0)
	v_pk_add_f32 v[2:3], v[2:3], v[4:5]
	s_nop 0
	v_pk_fma_f32 v[2:3], v[2:3], s[76:77], v[24:25] op_sel_hi:[1,0,0]
	s_nop 0
	v_mul_f32_e32 v4, 0x4b800000, v3
	v_cmp_gt_f32_e64 s[42:43], s55, v3
	v_cmp_gt_f32_e32 vcc, s55, v2
	s_nop 0
	v_cndmask_b32_e64 v3, v3, v4, s[42:43]
	v_rsq_f32_e32 v3, v3
	s_nop 0
	v_mul_f32_e32 v4, 0x45800000, v3
	v_cndmask_b32_e64 v3, v3, v4, s[42:43]
	v_mul_f32_e32 v4, 0x4b800000, v2
	v_cndmask_b32_e32 v2, v2, v4, vcc
	v_rsq_f32_e32 v2, v2
	v_mul_f32_e32 v10, v163, v3
	v_mul_f32_e32 v4, 0x45800000, v2
	v_cndmask_b32_e32 v2, v2, v4, vcc
	v_mul_f32_e32 v12, v163, v2
	v_add_u32_e32 v2, 0x80, v18
	v_mad_i64_i32 v[14:15], s[42:43], v2, s17, v[20:21]
	v_pk_mul_f32 v[2:3], v[94:95], v[6:7] op_sel_hi:[1,0]
	v_pk_mul_f32 v[4:5], v[96:97], v[6:7] op_sel_hi:[1,0]
	v_cvt_pk_bf16_f32 v2, v2, v3
	s_andn2_b64 vcc, exec, s[40:41]
	v_cvt_pk_bf16_f32 v3, v4, v5
	v_cvt_pk_bf16_f32 v4, v22, v23
	v_cvt_pk_bf16_f32 v5, v16, v17
	global_store_dwordx4 v[14:15], v[2:5], off
	v_pk_mul_f32 v[16:17], v[60:61], v[6:7] op_sel_hi:[1,0]
	s_nop 0
	v_pk_mul_f32 v[2:3], v[62:63], v[6:7] op_sel_hi:[1,0]
	v_pk_mul_f32 v[4:5], v[64:65], v[6:7] op_sel_hi:[1,0]
	v_cvt_pk_bf16_f32 v2, v2, v3
	v_pk_mul_f32 v[6:7], v[58:59], v[6:7] op_sel_hi:[1,0]
	v_cvt_pk_bf16_f32 v3, v4, v5
	s_nop 0
	v_cvt_pk_bf16_f32 v4, v6, v7
	v_cvt_pk_bf16_f32 v5, v16, v17
	global_store_dwordx4 v[14:15], v[2:5], off offset:256
	v_pk_mul_f32 v[14:15], v[84:85], v[8:9] op_sel_hi:[1,0]
	v_pk_mul_f32 v[16:17], v[82:83], v[8:9] op_sel_hi:[1,0]
	v_add_u32_e32 v2, 0x90, v18
	v_mad_i64_i32 v[6:7], s[42:43], v2, s17, v[20:21]
	v_pk_mul_f32 v[2:3], v[86:87], v[8:9] op_sel_hi:[1,0]
	v_pk_mul_f32 v[4:5], v[88:89], v[8:9] op_sel_hi:[1,0]
	v_cvt_pk_bf16_f32 v2, v2, v3
	s_nop 0
	v_cvt_pk_bf16_f32 v3, v4, v5
	v_cvt_pk_bf16_f32 v4, v16, v17
	v_cvt_pk_bf16_f32 v5, v14, v15
	global_store_dwordx4 v[6:7], v[2:5], off
	v_pk_mul_f32 v[14:15], v[52:53], v[8:9] op_sel_hi:[1,0]
	s_nop 0
	v_pk_mul_f32 v[2:3], v[54:55], v[8:9] op_sel_hi:[1,0]
	v_pk_mul_f32 v[4:5], v[56:57], v[8:9] op_sel_hi:[1,0]
	v_cvt_pk_bf16_f32 v2, v2, v3
	v_pk_mul_f32 v[8:9], v[50:51], v[8:9] op_sel_hi:[1,0]
	v_cvt_pk_bf16_f32 v3, v4, v5
	s_nop 0
	v_cvt_pk_bf16_f32 v4, v8, v9
	v_cvt_pk_bf16_f32 v5, v14, v15
	global_store_dwordx4 v[6:7], v[2:5], off offset:256
	v_pk_mul_f32 v[8:9], v[76:77], v[10:11] op_sel_hi:[1,0]
	v_pk_mul_f32 v[14:15], v[74:75], v[10:11] op_sel_hi:[1,0]
	v_add_u32_e32 v2, 0xa0, v18
	v_mad_i64_i32 v[6:7], s[42:43], v2, s17, v[20:21]
	v_pk_mul_f32 v[2:3], v[78:79], v[10:11] op_sel_hi:[1,0]
	v_pk_mul_f32 v[4:5], v[80:81], v[10:11] op_sel_hi:[1,0]
	v_cvt_pk_bf16_f32 v2, v2, v3
	s_nop 0
	v_cvt_pk_bf16_f32 v3, v4, v5
	v_cvt_pk_bf16_f32 v4, v14, v15
	v_cvt_pk_bf16_f32 v5, v8, v9
	global_store_dwordx4 v[6:7], v[2:5], off
	v_pk_mul_f32 v[8:9], v[44:45], v[10:11] op_sel_hi:[1,0]
	s_nop 0
	v_pk_mul_f32 v[2:3], v[46:47], v[10:11] op_sel_hi:[1,0]
	v_pk_mul_f32 v[4:5], v[48:49], v[10:11] op_sel_hi:[1,0]
	v_cvt_pk_bf16_f32 v2, v2, v3
	v_pk_mul_f32 v[10:11], v[42:43], v[10:11] op_sel_hi:[1,0]
	v_cvt_pk_bf16_f32 v3, v4, v5
	s_nop 0
	v_cvt_pk_bf16_f32 v4, v10, v11
	v_cvt_pk_bf16_f32 v5, v8, v9
	global_store_dwordx4 v[6:7], v[2:5], off offset:256
	v_pk_mul_f32 v[8:9], v[68:69], v[12:13] op_sel_hi:[1,0]
	v_pk_mul_f32 v[10:11], v[66:67], v[12:13] op_sel_hi:[1,0]
	v_add_u32_e32 v2, 0xb0, v18
	v_mad_i64_i32 v[6:7], s[42:43], v2, s17, v[20:21]
	v_pk_mul_f32 v[4:5], v[72:73], v[12:13] op_sel_hi:[1,0]
	v_pk_mul_f32 v[2:3], v[70:71], v[12:13] op_sel_hi:[1,0]
	s_nop 0
	v_cvt_pk_bf16_f32 v2, v2, v3
	v_cvt_pk_bf16_f32 v3, v4, v5
	v_cvt_pk_bf16_f32 v4, v10, v11
	v_cvt_pk_bf16_f32 v5, v8, v9
	global_store_dwordx4 v[6:7], v[2:5], off
	v_pk_mul_f32 v[8:9], v[36:37], v[12:13] op_sel_hi:[1,0]
	v_pk_mul_f32 v[10:11], v[34:35], v[12:13] op_sel_hi:[1,0]
	v_pk_mul_f32 v[4:5], v[40:41], v[12:13] op_sel_hi:[1,0]
	v_pk_mul_f32 v[2:3], v[38:39], v[12:13] op_sel_hi:[1,0]
	s_nop 0
	v_cvt_pk_bf16_f32 v2, v2, v3
	v_cvt_pk_bf16_f32 v3, v4, v5
	v_cvt_pk_bf16_f32 v4, v10, v11
	v_cvt_pk_bf16_f32 v5, v8, v9
	global_store_dwordx4 v[6:7], v[2:5], off offset:256
	s_cbranch_vccnz .LBB0_707
	s_andn2_b64 vcc, exec, s[58:59]
	s_cbranch_vccnz .LBB0_579
	s_barrier
	s_branch .LBB0_579
